# grid barrier: generation index by shift when the per-XCD workgroup count is 32 / the XCD count is 8 (was a ~25-instruction reciprocal division on the arrival critical path), full division kept as fall
# baseline (speedup 1.0000x reference)
.LBB0_209:
	s_or_b64 exec, exec, s[4:5]
	buffer_inv sc1
	s_waitcnt vmcnt(1)
	v_readfirstlane_b32 s2, v5
	v_sub_u32_e32 v6, 0, v4
	s_nop 0
	v_add_u32_e32 v5, s2, v3
	v_cmp_eq_u32_e32 vcc, 32, v4
	s_cbranch_vccz .Ldvs_19
	v_lshrrev_b32_e32 v3, 5, v5
	s_branch .Ldvd_19
.Ldvs_19:
	v_cvt_f32_u32_e32 v3, v4
	v_rcp_iflag_f32_e32 v3, v3
	s_nop 0
	v_mul_f32_e32 v3, 0x4f7ffffe, v3
	v_cvt_u32_f32_e32 v3, v3
	v_mul_lo_u32 v6, v6, v3
	v_mul_hi_u32 v6, v3, v6
	v_add_u32_e32 v3, v3, v6
	v_mul_hi_u32 v3, v5, v3
	v_mul_lo_u32 v6, v3, v4
	v_sub_u32_e32 v6, v5, v6
	v_cmp_ge_u32_e32 vcc, v6, v4
	v_add_u32_e32 v7, 1, v3
	s_nop 0
	v_cndmask_b32_e32 v3, v3, v7, vcc
	v_sub_u32_e32 v7, v6, v4
	v_cndmask_b32_e32 v6, v6, v7, vcc
	v_cmp_ge_u32_e32 vcc, v6, v4
	v_add_u32_e32 v6, 1, v3
	s_nop 0
	v_cndmask_b32_e32 v3, v3, v6, vcc
.Ldvd_19:
	v_add_u32_e32 v6, 1, v5
	v_mad_u64_u32 v[4:5], s[2:3], v4, v3, v[4:5]
	v_cmp_ne_u32_e32 vcc, v6, v4
	s_and_saveexec_b64 s[2:3], vcc
	s_xor_b64 s[2:3], exec, s[2:3]
	v_readlane_b32 s37, v253, 9
	s_cbranch_execz .LBB0_223
	s_waitcnt lgkmcnt(0)
	v_mov_b32_e32 v2, 0x2000
	global_load_dword v2, v2, s[0:1] offset:1024 sc1
	s_add_u32 s6, s0, 0x2400
	s_addc_u32 s7, s1, 0
	s_waitcnt vmcnt(0)
	v_cmp_eq_u32_e32 vcc, v2, v3
	s_and_saveexec_b64 s[4:5], vcc
	s_cbranch_execz .LBB0_222
	s_mov_b32 s18, 1
	s_mov_b64 s[8:9], 0
	s_branch .LBB0_213

.LBB0_226:
	s_or_b64 exec, exec, s[4:5]
	s_waitcnt vmcnt(0)
	v_readfirstlane_b32 s2, v4
	v_sub_u32_e32 v5, 0, v2
	v_add_u32_e32 v3, s2, v3
	s_mov_b64 s[4:5], -1
	v_cmp_eq_u32_e32 vcc, 8, v2
	s_cbranch_vccz .Ldvs_18
	v_lshrrev_b32_e32 v4, 3, v3
	s_branch .Ldvd_18
.Ldvs_18:
	v_cvt_f32_u32_e32 v4, v2
	v_rcp_iflag_f32_e32 v4, v4
	s_nop 0
	v_mul_f32_e32 v4, 0x4f7ffffe, v4
	v_cvt_u32_f32_e32 v4, v4
	v_mul_lo_u32 v5, v5, v4
	v_mul_hi_u32 v5, v4, v5
	v_add_u32_e32 v4, v4, v5
	v_mul_hi_u32 v4, v3, v4
	v_mul_lo_u32 v5, v4, v2
	v_sub_u32_e32 v5, v3, v5
	v_cmp_ge_u32_e32 vcc, v5, v2
	v_add_u32_e32 v6, 1, v4
	s_nop 0
	v_cndmask_b32_e32 v4, v4, v6, vcc
	v_sub_u32_e32 v6, v5, v2
	v_cndmask_b32_e32 v5, v5, v6, vcc
	v_cmp_ge_u32_e32 vcc, v5, v2
	v_add_u32_e32 v5, 1, v4
	s_nop 0
	v_cndmask_b32_e32 v4, v4, v5, vcc
.Ldvd_18:
	v_add_u32_e32 v5, 1, v3
	v_mad_u64_u32 v[2:3], s[2:3], v2, v4, v[2:3]
	v_readlane_b32 s2, v254, 27
	v_readlane_b32 s3, v254, 28
	v_cmp_ne_u32_e32 vcc, v5, v2
	s_nop 0
	v_mov_b64_e32 v[2:3], s[2:3]
	s_and_saveexec_b64 s[2:3], vcc
	s_cbranch_execz .LBB0_238
	v_readlane_b32 s4, v254, 27
	v_readlane_b32 s5, v254, 28
	s_mov_b64 s[6:7], 0
	s_nop 3
	global_load_dword v2, v195, s[4:5] sc1
	s_waitcnt vmcnt(0)
	v_cmp_eq_u32_e32 vcc, v2, v4
	s_and_saveexec_b64 s[4:5], vcc
	s_cbranch_execz .LBB0_237
	s_mov_b32 s16, 1
	s_branch .LBB0_230

.LBB0_334:
	s_or_b64 exec, exec, s[6:7]
	s_waitcnt vmcnt(0)
	v_readfirstlane_b32 s4, v4
	v_sub_u32_e32 v5, 0, v2
	v_add_u32_e32 v3, s4, v3
	s_mov_b64 s[6:7], -1
	v_cmp_eq_u32_e32 vcc, 8, v2
	s_cbranch_vccz .Ldvs_16
	v_lshrrev_b32_e32 v4, 3, v3
	s_branch .Ldvd_16

.Ldvd_16:
	v_add_u32_e32 v5, 1, v3
	v_mad_u64_u32 v[2:3], s[4:5], v2, v4, v[2:3]
	v_readlane_b32 s4, v254, 27
	v_readlane_b32 s5, v254, 28
	v_cmp_ne_u32_e32 vcc, v5, v2
	s_nop 0
	v_mov_b64_e32 v[2:3], s[4:5]
	s_and_saveexec_b64 s[4:5], vcc
	s_cbranch_execz .LBB0_346
	v_readlane_b32 s6, v254, 27
	v_readlane_b32 s7, v254, 28
	s_mov_b64 s[8:9], 0
	s_nop 3
	global_load_dword v2, v195, s[6:7] sc1
	s_waitcnt vmcnt(0)
	v_cmp_eq_u32_e32 vcc, v2, v4
	s_and_saveexec_b64 s[6:7], vcc
	s_cbranch_execz .LBB0_345
	s_mov_b32 s18, 1
	s_branch .LBB0_338

.Ldvd_7:
	v_add_u32_e32 v6, 1, v5
	v_mad_u64_u32 v[4:5], s[2:3], v4, v3, v[4:5]
	v_cmp_ne_u32_e32 vcc, v6, v4
	s_and_saveexec_b64 s[2:3], vcc
	s_xor_b64 s[2:3], exec, s[2:3]
	s_cbranch_execz .LBB0_766
	s_waitcnt lgkmcnt(0)
	v_mov_b32_e32 v2, 0x2000
	global_load_dword v2, v2, s[0:1] offset:1024 sc1
	s_add_u32 s6, s0, 0x2400
	s_addc_u32 s7, s1, 0
	s_waitcnt vmcnt(0)
	v_cmp_eq_u32_e32 vcc, v2, v3
	s_and_saveexec_b64 s[4:5], vcc
	s_cbranch_execz .LBB0_765
	s_mov_b32 s18, 1
	s_mov_b64 s[8:9], 0
	s_branch .LBB0_756

.LBB0_912:
	s_or_b64 exec, exec, s[4:5]
	s_waitcnt vmcnt(0)
	v_readfirstlane_b32 s2, v5
	v_sub_u32_e32 v6, 0, v4
	s_nop 0
	v_add_u32_e32 v5, s2, v3
	v_cmp_eq_u32_e32 vcc, 32, v4
	s_cbranch_vccz .Ldvs_5
	v_lshrrev_b32_e32 v3, 5, v5
	s_branch .Ldvd_5
